# v73 stack + block-compression GEMM epilogue: the four position-bias quads loaded once instead of eight load+drain round trips
# baseline (speedup 1.0000x reference)
.LBB0_1456:
	v_lshl_add_u64 v[72:73], v[68:69], 0, s[4:5]
	v_add_co_u32_e32 v56, vcc, s27, v72
	v_lshl_add_u64 v[150:151], v[70:71], 0, s[4:5]
	s_nop 0
	v_addc_co_u32_e32 v57, vcc, 0, v73, vcc
	ds_read_b64_tr_b16 v[60:61], v119
	ds_read_b64_tr_b16 v[62:63], v120
	ds_read_b128 v[122:125], v79
	ds_read_b64_tr_b16 v[126:127], v116
	ds_read_b64_tr_b16 v[128:129], v113
	global_load_dwordx4 v[130:133], v[56:57], off offset:3328
	v_add_co_u32_e32 v56, vcc, s27, v150
	ds_read_b128 v[134:137], v79 offset:2304
	s_nop 0
	v_addc_co_u32_e32 v57, vcc, 0, v151, vcc
	s_mov_b32 s9, 0xffff2000
	v_add_co_u32_e32 v146, vcc, s9, v66
	s_mov_b32 s9, 0xffff4000
	s_nop 0
	v_addc_co_u32_e32 v147, vcc, -1, v67, vcc
	v_add_co_u32_e32 v148, vcc, s9, v66
	ds_read_b64_tr_b16 v[138:139], v115
	ds_read_b64_tr_b16 v[140:141], v114
	ds_read_b64_tr_b16 v[142:143], v118
	ds_read_b64_tr_b16 v[144:145], v117
	v_addc_co_u32_e32 v149, vcc, -1, v67, vcc
	s_mov_b32 s9, 0xffff6000
	s_waitcnt lgkmcnt(7)
	v_mfma_f32_16x16x32_bf16 v[52:55], v[60:63], v[122:125], v[52:55]
	global_load_dwordx4 v[56:59], v[56:57], off offset:3328
	s_waitcnt lgkmcnt(4)
	v_mfma_f32_16x16x32_bf16 v[36:39], v[60:63], v[134:137], v[36:39]
	v_add_co_u32_e32 v60, vcc, s9, v66
	s_movk_i32 s9, 0x8000
	s_nop 0
	v_addc_co_u32_e32 v61, vcc, -1, v67, vcc
	v_add_co_u32_e32 v62, vcc, s9, v66
	v_mfma_f32_16x16x32_bf16 v[48:51], v[126:129], v[122:125], v[48:51]
	s_nop 0
	v_addc_co_u32_e32 v63, vcc, -1, v67, vcc
	s_waitcnt lgkmcnt(2)
	v_mfma_f32_16x16x32_bf16 v[44:47], v[138:141], v[122:125], v[44:47]
	s_waitcnt lgkmcnt(0)
	v_mfma_f32_16x16x32_bf16 v[40:43], v[142:145], v[122:125], v[40:43]
	global_load_dwordx4 v[122:125], v[146:147], off
	s_nop 0
	global_load_dwordx4 v[146:149], v[148:149], off
	v_mfma_f32_16x16x32_bf16 v[32:35], v[126:129], v[134:137], v[32:35]
	v_mfma_f32_16x16x32_bf16 v[126:129], v[138:141], v[134:137], v[28:31]
	s_nop 2
	global_load_dwordx4 v[28:31], v[60:61], off
	s_nop 0
	global_load_dwordx4 v[60:63], v[62:63], off
	s_waitcnt vmcnt(11)
	ds_write_b128 v80, v[12:15] offset:46080
	s_waitcnt vmcnt(9)
	v_cvt_pk_bf16_f32 v12, v20, v21
	v_mfma_f32_16x16x32_bf16 v[24:27], v[142:145], v[134:137], v[24:27]
	v_cvt_pk_bf16_f32 v13, v22, v23
	ds_write_b64 v109, v[12:13]
	s_waitcnt vmcnt(8)
	v_cvt_pk_bf16_f32 v12, v16, v17
	v_cvt_pk_bf16_f32 v13, v18, v19
	ds_write_b64 v105, v[12:13]
	ds_read_b64_tr_b16 v[12:13], v106
	ds_read_b64_tr_b16 v[14:15], v107
	ds_read_b128 v[16:19], v79 offset:64
	ds_read_b64_tr_b16 v[20:21], v104
	ds_read_b64_tr_b16 v[22:23], v102
	ds_read_b64_tr_b16 v[134:135], v103
	ds_read_b64_tr_b16 v[136:137], v100
	ds_read_b64_tr_b16 v[138:139], v101
	ds_read_b64_tr_b16 v[140:141], v99
	s_waitcnt lgkmcnt(6)
	v_mfma_f32_16x16x32_bf16 v[52:55], v[12:15], v[16:19], v[52:55]
	s_waitcnt lgkmcnt(4)
	v_mfma_f32_16x16x32_bf16 v[48:51], v[20:23], v[16:19], v[48:51]
	s_waitcnt lgkmcnt(2)
	v_mfma_f32_16x16x32_bf16 v[44:47], v[134:137], v[16:19], v[44:47]
	s_waitcnt lgkmcnt(0)
	v_mfma_f32_16x16x32_bf16 v[16:19], v[138:141], v[16:19], v[40:43]
	s_nop 2
	ds_read_b128 v[40:43], v79 offset:2368
	s_waitcnt lgkmcnt(0)
	v_mfma_f32_16x16x32_bf16 v[36:39], v[12:15], v[40:43], v[36:39]
	ds_write_b128 v80, v[0:3] offset:55296
	s_waitcnt vmcnt(7)
	v_cvt_pk_bf16_f32 v0, v8, v9
	v_cvt_pk_bf16_f32 v1, v10, v11
	v_mfma_f32_16x16x32_bf16 v[32:35], v[20:23], v[40:43], v[32:35]
	ds_write_b64 v98, v[0:1]
	s_waitcnt vmcnt(6)
	v_cvt_pk_bf16_f32 v0, v4, v5
	v_cvt_pk_bf16_f32 v1, v6, v7
	v_mfma_f32_16x16x32_bf16 v[8:11], v[134:137], v[40:43], v[126:129]
	ds_write_b64 v97, v[0:1]
	v_mfma_f32_16x16x32_bf16 v[24:27], v[138:141], v[40:43], v[24:27]
	s_waitcnt lgkmcnt(0)
	s_barrier
	ds_read_b64_tr_b16 v[4:5], v95
	ds_read_b64_tr_b16 v[6:7], v96
	ds_read_b128 v[20:23], v79 offset:46080
	ds_read_b64_tr_b16 v[40:41], v94
	ds_read_b64_tr_b16 v[42:43], v92
	ds_read_b128 v[126:129], v79 offset:48384
	ds_read_b64_tr_b16 v[134:135], v93
	ds_read_b64_tr_b16 v[136:137], v90
	ds_read_b64_tr_b16 v[138:139], v91
	ds_read_b64_tr_b16 v[140:141], v89
	v_add_co_u32_e32 v0, vcc, s28, v72
	s_movk_i32 s9, 0xa000
	s_nop 0
	v_addc_co_u32_e32 v1, vcc, 0, v73, vcc
	global_load_dwordx4 v[12:15], v[0:1], off offset:256
	v_add_co_u32_e32 v0, vcc, s28, v150
	s_waitcnt lgkmcnt(0)
	v_mfma_f32_16x16x32_bf16 v[142:145], v[138:141], v[20:23], v[16:19]
	v_addc_co_u32_e32 v1, vcc, 0, v151, vcc
	global_load_dwordx4 v[0:3], v[0:1], off offset:256
	s_nop 0
	v_add_co_u32_e32 v16, vcc, s9, v66
	s_movk_i32 s9, 0xc000
	s_nop 0
	v_addc_co_u32_e32 v17, vcc, -1, v67, vcc
	v_mfma_f32_16x16x32_bf16 v[52:55], v[4:7], v[20:23], v[52:55]
	v_mfma_f32_16x16x32_bf16 v[36:39], v[4:7], v[126:129], v[36:39]
	v_add_co_u32_e32 v4, vcc, s9, v66
	s_movk_i32 s9, 0xe000
	s_nop 0
	v_addc_co_u32_e32 v5, vcc, -1, v67, vcc
	v_mfma_f32_16x16x32_bf16 v[48:51], v[40:43], v[20:23], v[48:51]
	v_mfma_f32_16x16x32_bf16 v[44:47], v[134:137], v[20:23], v[44:47]
	global_load_dwordx4 v[20:23], v[16:17], off
	s_nop 0
	global_load_dwordx4 v[16:19], v[4:5], off
	v_add_co_u32_e32 v4, vcc, s9, v66
	v_mfma_f32_16x16x32_bf16 v[134:137], v[134:137], v[126:129], v[8:11]
	s_nop 0
	v_addc_co_u32_e32 v5, vcc, -1, v67, vcc
	s_nop 0
	global_load_dwordx4 v[8:11], v[4:5], off
	s_nop 0
	global_load_dwordx4 v[4:7], v[66:67], off
	v_mfma_f32_16x16x32_bf16 v[32:35], v[40:43], v[126:129], v[32:35]
	s_waitcnt vmcnt(9)
	v_cvt_pk_bf16_f32 v40, v122, v123
	v_cvt_pk_bf16_f32 v41, v124, v125
	ds_write_b128 v80, v[130:133]
	v_mfma_f32_16x16x32_bf16 v[24:27], v[138:141], v[126:129], v[24:27]
	ds_write_b64 v108, v[40:41]
	s_waitcnt vmcnt(8)
	v_cvt_pk_bf16_f32 v40, v146, v147
	v_cvt_pk_bf16_f32 v41, v148, v149
	ds_write_b64 v110, v[40:41]
	ds_read_b64_tr_b16 v[122:123], v87
	ds_read_b64_tr_b16 v[124:125], v88
	ds_read_b128 v[40:43], v79 offset:46144
	ds_read_b64_tr_b16 v[126:127], v86
	ds_read_b64_tr_b16 v[128:129], v84
	ds_read_b64_tr_b16 v[130:131], v85
	ds_read_b64_tr_b16 v[132:133], v82
	ds_read_b64_tr_b16 v[138:139], v83
	ds_read_b64_tr_b16 v[140:141], v81
	s_waitcnt lgkmcnt(6)
	v_mfma_f32_16x16x32_bf16 v[52:55], v[122:125], v[40:43], v[52:55]
	s_waitcnt lgkmcnt(4)
	v_mfma_f32_16x16x32_bf16 v[48:51], v[126:129], v[40:43], v[48:51]
	s_waitcnt lgkmcnt(2)
	v_mfma_f32_16x16x32_bf16 v[44:47], v[130:133], v[40:43], v[44:47]
	s_waitcnt lgkmcnt(0)
	v_mfma_f32_16x16x32_bf16 v[40:43], v[138:141], v[40:43], v[142:145]
	s_nop 2
	ds_read_b128 v[142:145], v79 offset:48448
	s_waitcnt lgkmcnt(0)
	v_mfma_f32_16x16x32_bf16 v[36:39], v[122:125], v[142:145], v[36:39]
	ds_write_b128 v80, v[56:59] offset:9216
	s_waitcnt vmcnt(7)
	v_cvt_pk_bf16_f32 v56, v28, v29
	v_cvt_pk_bf16_f32 v57, v30, v31
	v_mfma_f32_16x16x32_bf16 v[32:35], v[126:129], v[142:145], v[32:35]
	ds_write_b64 v111, v[56:57]
	s_waitcnt vmcnt(6)
	v_cvt_pk_bf16_f32 v56, v60, v61
	v_cvt_pk_bf16_f32 v57, v62, v63
	v_mfma_f32_16x16x32_bf16 v[28:31], v[130:133], v[142:145], v[134:137]
	ds_write_b64 v112, v[56:57]
	v_mfma_f32_16x16x32_bf16 v[24:27], v[138:141], v[142:145], v[24:27]
	s_add_i32 s8, s8, 2
	s_mov_b64 s[10:11], 0x10000
	v_lshl_add_u64 v[66:67], v[66:67], 0, s[10:11]
	v_lshl_add_u64 v[68:69], v[68:69], 0, s[6:7]
	s_cmp_lt_u32 s8, 28
	v_lshl_add_u64 v[70:71], v[70:71], 0, s[6:7]
	s_waitcnt lgkmcnt(0)
	s_barrier
	s_cbranch_scc1 .LBB0_1456
	ds_read_b64_tr_b16 v[56:57], v119
	ds_read_b64_tr_b16 v[58:59], v120
	ds_read_b128 v[60:63], v79
	ds_read_b64_tr_b16 v[66:67], v116
	ds_read_b64_tr_b16 v[68:69], v113
	ds_read_b64_tr_b16 v[70:71], v115
	ds_read_b64_tr_b16 v[72:73], v114
	ds_read_b64_tr_b16 v[110:111], v118
	ds_read_b64_tr_b16 v[112:113], v117
	s_waitcnt lgkmcnt(6)
	v_mfma_f32_16x16x32_bf16 v[52:55], v[56:59], v[60:63], v[52:55]
	s_waitcnt vmcnt(2)
	v_cvt_pk_bf16_f32 v16, v16, v17
	v_cvt_pk_bf16_f32 v17, v18, v19
	v_and_b32_e32 v64, 64, v78
	s_waitcnt lgkmcnt(4)
	v_mfma_f32_16x16x32_bf16 v[48:51], v[66:69], v[60:63], v[48:51]
	s_ashr_i32 s8, s39, 5
	v_cvt_pk_bf16_f32 v20, v20, v21
	v_cvt_pk_bf16_f32 v21, v22, v23
	s_waitcnt lgkmcnt(2)
	v_mfma_f32_16x16x32_bf16 v[44:47], v[70:73], v[60:63], v[44:47]
	s_waitcnt lgkmcnt(0)
	v_mfma_f32_16x16x32_bf16 v[40:43], v[110:113], v[60:63], v[40:43]
	ds_read_b128 v[60:63], v79 offset:2304
	ds_write_b128 v80, v[12:15] offset:46080
	ds_write_b64 v105, v[16:17]
	s_waitcnt lgkmcnt(2)
	v_mfma_f32_16x16x32_bf16 v[36:39], v[56:59], v[60:63], v[36:39]
	ds_write_b64 v109, v[20:21]
	v_mfma_f32_16x16x32_bf16 v[32:35], v[66:69], v[60:63], v[32:35]
	v_mfma_f32_16x16x32_bf16 v[12:15], v[70:73], v[60:63], v[28:31]
	v_mfma_f32_16x16x32_bf16 v[16:19], v[110:113], v[60:63], v[24:27]
	ds_read_b64_tr_b16 v[20:21], v106
	ds_read_b64_tr_b16 v[22:23], v107
	s_nop 0
	ds_read_b128 v[24:27], v79 offset:64
	ds_read_b64_tr_b16 v[28:29], v104
	ds_read_b64_tr_b16 v[30:31], v102
	ds_read_b64_tr_b16 v[56:57], v103
	ds_read_b64_tr_b16 v[58:59], v100
	ds_read_b64_tr_b16 v[60:61], v101
	ds_read_b64_tr_b16 v[62:63], v99
	s_waitcnt lgkmcnt(6)
	v_mfma_f32_16x16x32_bf16 v[52:55], v[20:23], v[24:27], v[52:55]
	s_waitcnt vmcnt(0)
	v_cvt_pk_bf16_f32 v4, v4, v5
	v_cvt_pk_bf16_f32 v5, v6, v7
	v_cvt_pk_bf16_f32 v8, v8, v9
	s_waitcnt lgkmcnt(4)
	v_mfma_f32_16x16x32_bf16 v[48:51], v[28:31], v[24:27], v[48:51]
	v_cvt_pk_bf16_f32 v9, v10, v11
	s_waitcnt lgkmcnt(2)
	v_mfma_f32_16x16x32_bf16 v[44:47], v[56:59], v[24:27], v[44:47]
	s_waitcnt lgkmcnt(0)
	v_mfma_f32_16x16x32_bf16 v[24:27], v[60:63], v[24:27], v[40:43]
	s_nop 2
	ds_read_b128 v[40:43], v79 offset:2368
	s_waitcnt lgkmcnt(0)
	v_mfma_f32_16x16x32_bf16 v[20:23], v[20:23], v[40:43], v[36:39]
	ds_write_b128 v80, v[0:3] offset:55296
	ds_write_b64 v97, v[4:5]
	ds_write_b64 v98, v[8:9]
	v_mfma_f32_16x16x32_bf16 v[28:31], v[28:31], v[40:43], v[32:35]
	v_mfma_f32_16x16x32_bf16 v[0:3], v[56:59], v[40:43], v[12:15]
	v_mfma_f32_16x16x32_bf16 v[4:7], v[60:63], v[40:43], v[16:19]
	s_waitcnt lgkmcnt(0)
	s_barrier
	ds_read_b64_tr_b16 v[8:9], v95
	ds_read_b64_tr_b16 v[10:11], v96
	ds_read_b128 v[12:15], v79 offset:46080
	ds_read_b64_tr_b16 v[16:17], v94
	ds_read_b64_tr_b16 v[18:19], v92
	ds_read_b64_tr_b16 v[36:37], v93
	s_waitcnt lgkmcnt(1)
	v_mfma_f32_16x16x32_bf16 v[40:43], v[16:19], v[12:15], v[48:51]
	ds_read_b64_tr_b16 v[38:39], v90
	s_nop 1
	ds_read_b64_tr_b16 v[48:49], v91
	ds_read_b64_tr_b16 v[50:51], v89
	v_mfma_f32_16x16x32_bf16 v[32:35], v[8:11], v[12:15], v[52:55]
	s_waitcnt lgkmcnt(2)
	v_mfma_f32_16x16x32_bf16 v[44:47], v[36:39], v[12:15], v[44:47]
	s_waitcnt lgkmcnt(0)
	v_mfma_f32_16x16x32_bf16 v[12:15], v[48:51], v[12:15], v[24:27]
	s_nop 2
	ds_read_b128 v[24:27], v79 offset:48384
	s_waitcnt lgkmcnt(0)
	v_mfma_f32_16x16x32_bf16 v[8:11], v[8:11], v[24:27], v[20:23]
	v_mfma_f32_16x16x32_bf16 v[0:3], v[36:39], v[24:27], v[0:3]
	v_mfma_f32_16x16x32_bf16 v[36:39], v[48:51], v[24:27], v[4:7]
	v_mfma_f32_16x16x32_bf16 v[52:55], v[16:19], v[24:27], v[28:31]
	s_nop 1
	ds_read_b64_tr_b16 v[4:5], v87
	ds_read_b64_tr_b16 v[6:7], v88
	ds_read_b128 v[16:19], v79 offset:46144
	ds_read_b64_tr_b16 v[48:49], v86
	s_waitcnt lgkmcnt(1)
	v_mfma_f32_16x16x32_bf16 v[28:31], v[4:7], v[16:19], v[32:35]
	ds_read_b64_tr_b16 v[50:51], v84
	s_nop 1
	ds_read_b64_tr_b16 v[32:33], v85
	s_waitcnt lgkmcnt(1)
	v_mfma_f32_16x16x32_bf16 v[24:27], v[48:51], v[16:19], v[40:43]
	ds_read_b64_tr_b16 v[34:35], v82
	s_nop 1
	ds_read_b64_tr_b16 v[40:41], v83
	ds_read_b64_tr_b16 v[42:43], v81
	s_waitcnt lgkmcnt(2)
	v_mfma_f32_16x16x32_bf16 v[20:23], v[32:35], v[16:19], v[44:47]
	s_nop 2
	ds_read_b128 v[44:47], v79 offset:48448
	s_waitcnt lgkmcnt(1)
	v_mfma_f32_16x16x32_bf16 v[16:19], v[40:43], v[16:19], v[12:15]
	s_waitcnt lgkmcnt(0)
	v_mfma_f32_16x16x32_bf16 v[12:15], v[4:7], v[44:47], v[8:11]
	v_mfma_f32_16x16x32_bf16 v[8:11], v[48:51], v[44:47], v[52:55]
	v_mfma_f32_16x16x32_bf16 v[4:7], v[32:35], v[44:47], v[0:3]
	v_mfma_f32_16x16x32_bf16 v[0:3], v[40:43], v[44:47], v[36:39]
	s_lshl_b32 s10, s8, 7
	s_ashr_i32 s11, s10, 31
	v_lshrrev_b32_e32 v32, 2, v78
	s_lshl_b64 s[10:11], s[10:11], 2
	v_and_or_b32 v38, v32, 12, v64
	s_add_u32 s10, s34, s10
	s_addc_u32 s11, s35, s11
	v_lshlrev_b32_e32 v64, 2, v38
	s_barrier
	global_load_dwordx4 v[160:163], v64, s[10:11]
	global_load_dwordx4 v[164:167], v64, s[10:11] offset:64
	global_load_dwordx4 v[168:171], v64, s[10:11] offset:128
	global_load_dwordx4 v[172:175], v64, s[10:11] offset:192
	s_waitcnt vmcnt(0)
	v_mov_b32_e32 v32, v160
	v_mov_b32_e32 v33, v161
	v_mov_b32_e32 v34, v162
	v_mov_b32_e32 v35, v163
	v_add_f32_e32 v28, v28, v32
	v_mul_f32_e32 v32, 0x3d372713, v28
	v_mul_f32_e32 v32, v28, v32
	v_fma_f32 v32, v28, v32, v28
	v_mul_f32_e32 v36, 0x3f4c422a, v32
	v_cmp_nlt_f32_e64 s[12:13], |v36|, s29
	s_and_saveexec_b64 s[42:43], s[12:13]
	s_xor_b64 s[12:13], exec, s[42:43]
	s_cbranch_execz .LBB0_1459
	v_add_f32_e64 v32, |v36|, |v36|
	v_mul_f32_e32 v37, 0x3fb8aa3b, v32
	v_rndne_f32_e32 v39, v37
	v_sub_f32_e32 v40, v37, v39
	v_fma_f32 v37, v32, s33, -v37
	v_fmac_f32_e32 v37, 0x32a5705f, v32
	v_add_f32_e32 v37, v40, v37
	v_cvt_i32_f32_e32 v39, v39
	v_exp_f32_e32 v37, v37
	v_cmp_ngt_f32_e32 vcc, s36, v32
	v_ldexp_f32 v37, v37, v39
	s_nop 0
	v_cndmask_b32_e32 v37, 0, v37, vcc
	v_cmp_nlt_f32_e32 vcc, s37, v32
	s_nop 1
	v_cndmask_b32_e32 v32, v77, v37, vcc
	v_add_f32_e32 v32, 1.0, v32
	v_rcp_f32_e32 v32, v32
	s_nop 0
	v_fma_f32 v37, v32, -2.0, 1.0

.LBB0_1471:
	s_andn2_saveexec_b64 s[12:13], s[12:13]
	v_mul_f32_e32 v32, v41, v41
	v_fmamk_f32 v33, v32, 0xbbbac73d, v75
	v_fmaak_f32 v33, v32, v33, 0xbd5c1c4e
	v_fmaak_f32 v33, v32, v33, 0x3e088382
	v_fmaak_f32 v33, v32, v33, 0xbeaaaa99
	v_mul_f32_e64 v33, |v41|, v33
	v_fma_f32 v43, v32, v33, |v41|
	s_or_b64 exec, exec, s[12:13]
	v_bfi_b32 v34, s38, v42, v34
	v_mul_f32_e32 v30, 0.5, v30
	v_add_f32_e32 v34, 1.0, v34
	v_mul_f32_e32 v30, v30, v34
	v_bfi_b32 v34, s38, v40, v39
	v_mul_f32_e32 v29, 0.5, v29
	v_add_f32_e32 v34, 1.0, v34
	v_mul_f32_e32 v39, v29, v34
	v_bfi_b32 v29, s38, v37, v36
	v_mul_f32_e32 v28, 0.5, v28
	v_add_f32_e32 v29, 1.0, v29
	v_mul_f32_e32 v40, v28, v29
	v_ashrrev_i32_e32 v28, 2, v78
	v_and_b32_e32 v37, 0xffffffe0, v28
	v_and_b32_e32 v36, 15, v78
	v_add_u32_e32 v28, s40, v37
	s_ashr_i32 s9, s8, 31
	v_lshl_add_u64 v[32:33], s[10:11], 0, v[64:65]
	v_or_b32_e32 v28, v28, v36
	s_lshl_b64 s[10:11], s[8:9], 20
	v_ashrrev_i32_e32 v29, 31, v28
	s_add_u32 s10, s2, s10
	s_addc_u32 s11, s3, s11
	v_lshlrev_b64 v[28:29], 8, v[28:29]
	v_lshl_add_u64 v[28:29], s[10:11], 0, v[28:29]
	v_lshlrev_b32_e32 v64, 1, v38
	v_lshl_add_u64 v[34:35], v[28:29], 0, v[64:65]
	v_bfi_b32 v29, s38, v43, v41
	v_mul_f32_e32 v28, 0.5, v31
	v_add_f32_e32 v29, 1.0, v29
	v_mul_f32_e32 v29, v28, v29
	v_cvt_pk_bf16_f32 v28, v40, v39
	v_cvt_pk_bf16_f32 v29, v30, v29
	global_store_dwordx2 v[34:35], v[28:29], off
	v_mov_b32_e32 v28, v164
	v_mov_b32_e32 v29, v165
	v_mov_b32_e32 v30, v166
	v_mov_b32_e32 v31, v167
	v_add_f32_e32 v24, v24, v28
	v_mul_f32_e32 v28, 0x3d372713, v24
	v_mul_f32_e32 v28, v24, v28
	v_fma_f32 v28, v24, v28, v24
	v_mul_f32_e32 v28, 0x3f4c422a, v28
	v_cmp_nlt_f32_e64 s[12:13], |v28|, s29
	s_and_saveexec_b64 s[42:43], s[12:13]
	s_xor_b64 s[12:13], exec, s[42:43]
	s_cbranch_execz .LBB0_1475
	v_add_f32_e64 v38, |v28|, |v28|
	v_mul_f32_e32 v39, 0x3fb8aa3b, v38
	v_rndne_f32_e32 v40, v39
	v_sub_f32_e32 v41, v39, v40
	v_fma_f32 v39, v38, s33, -v39
	v_fmac_f32_e32 v39, 0x32a5705f, v38
	v_add_f32_e32 v39, v41, v39
	v_cvt_i32_f32_e32 v40, v40
	v_exp_f32_e32 v39, v39
	v_cmp_ngt_f32_e32 vcc, s36, v38
	v_ldexp_f32 v39, v39, v40
	s_nop 0
	v_cndmask_b32_e32 v39, 0, v39, vcc
	v_cmp_nlt_f32_e32 vcc, s37, v38
	s_nop 1
	v_cndmask_b32_e32 v38, v77, v39, vcc
	v_add_f32_e32 v38, 1.0, v38
	v_rcp_f32_e32 v38, v38
	s_nop 0
	v_fma_f32 v38, v38, -2.0, 1.0

.LBB0_1487:
	s_andn2_saveexec_b64 s[12:13], s[12:13]
	v_mul_f32_e32 v41, v31, v31
	v_fmamk_f32 v42, v41, 0xbbbac73d, v75
	v_fmaak_f32 v42, v41, v42, 0xbd5c1c4e
	v_fmaak_f32 v42, v41, v42, 0x3e088382
	v_fmaak_f32 v42, v41, v42, 0xbeaaaa99
	v_mul_f32_e64 v42, |v31|, v42
	v_fma_f32 v41, v41, v42, |v31|
	s_or_b64 exec, exec, s[12:13]
	v_bfi_b32 v28, s38, v38, v28
	v_mul_f32_e32 v24, 0.5, v24
	v_add_f32_e32 v28, 1.0, v28
	v_bfi_b32 v30, s38, v40, v30
	v_bfi_b32 v29, s38, v39, v29
	v_mul_f32_e32 v24, v24, v28
	v_bfi_b32 v28, s38, v41, v31
	v_mul_f32_e32 v26, 0.5, v26
	v_add_f32_e32 v30, 1.0, v30
	v_mul_f32_e32 v25, 0.5, v25
	v_add_f32_e32 v29, 1.0, v29
	v_mul_f32_e32 v27, 0.5, v27
	v_add_f32_e32 v28, 1.0, v28
	v_mul_f32_e32 v26, v26, v30
	v_mul_f32_e32 v25, v25, v29
	v_mul_f32_e32 v27, v27, v28
	v_cvt_pk_bf16_f32 v24, v24, v25
	v_cvt_pk_bf16_f32 v25, v26, v27
	global_store_dwordx2 v[34:35], v[24:25], off offset:32
	v_mov_b32_e32 v24, v168
	v_mov_b32_e32 v25, v169
	v_mov_b32_e32 v26, v170
	v_mov_b32_e32 v27, v171
	v_add_f32_e32 v20, v20, v24
	v_mul_f32_e32 v24, 0x3d372713, v20
	v_mul_f32_e32 v24, v20, v24
	v_fma_f32 v24, v20, v24, v20
	v_mul_f32_e32 v24, 0x3f4c422a, v24
	v_cmp_nlt_f32_e64 s[12:13], |v24|, s29
	s_and_saveexec_b64 s[42:43], s[12:13]
	s_xor_b64 s[12:13], exec, s[42:43]
	s_cbranch_execz .LBB0_1491
	v_add_f32_e64 v28, |v24|, |v24|
	v_mul_f32_e32 v29, 0x3fb8aa3b, v28
	v_rndne_f32_e32 v30, v29
	v_sub_f32_e32 v31, v29, v30
	v_fma_f32 v29, v28, s33, -v29
	v_fmac_f32_e32 v29, 0x32a5705f, v28
	v_add_f32_e32 v29, v31, v29
	v_cvt_i32_f32_e32 v30, v30
	v_exp_f32_e32 v29, v29
	v_cmp_ngt_f32_e32 vcc, s36, v28
	v_ldexp_f32 v29, v29, v30
	s_nop 0
	v_cndmask_b32_e32 v29, 0, v29, vcc
	v_cmp_nlt_f32_e32 vcc, s37, v28
	s_nop 1
	v_cndmask_b32_e32 v28, v77, v29, vcc
	v_add_f32_e32 v28, 1.0, v28
	v_rcp_f32_e32 v28, v28
	s_nop 0
	v_fma_f32 v28, v28, -2.0, 1.0

.LBB0_1503:
	s_andn2_saveexec_b64 s[12:13], s[12:13]
	v_mul_f32_e32 v31, v27, v27
	v_fmamk_f32 v38, v31, 0xbbbac73d, v75
	v_fmaak_f32 v38, v31, v38, 0xbd5c1c4e
	v_fmaak_f32 v38, v31, v38, 0x3e088382
	v_fmaak_f32 v38, v31, v38, 0xbeaaaa99
	v_mul_f32_e64 v38, |v27|, v38
	v_fma_f32 v31, v31, v38, |v27|
	s_or_b64 exec, exec, s[12:13]
	v_bfi_b32 v24, s38, v28, v24
	v_mul_f32_e32 v20, 0.5, v20
	v_add_f32_e32 v24, 1.0, v24
	v_bfi_b32 v26, s38, v30, v26
	v_bfi_b32 v25, s38, v29, v25
	v_mul_f32_e32 v20, v20, v24
	v_bfi_b32 v24, s38, v31, v27
	v_mul_f32_e32 v22, 0.5, v22
	v_add_f32_e32 v26, 1.0, v26
	v_mul_f32_e32 v21, 0.5, v21
	v_add_f32_e32 v25, 1.0, v25
	v_mul_f32_e32 v23, 0.5, v23
	v_add_f32_e32 v24, 1.0, v24
	v_mul_f32_e32 v22, v22, v26
	v_mul_f32_e32 v21, v21, v25
	v_mul_f32_e32 v23, v23, v24
	v_cvt_pk_bf16_f32 v20, v20, v21
	v_cvt_pk_bf16_f32 v21, v22, v23
	global_store_dwordx2 v[34:35], v[20:21], off offset:64
	v_mov_b32_e32 v20, v172
	v_mov_b32_e32 v21, v173
	v_mov_b32_e32 v22, v174
	v_mov_b32_e32 v23, v175
	v_add_f32_e32 v16, v16, v20
	v_mul_f32_e32 v20, 0x3d372713, v16
	v_mul_f32_e32 v20, v16, v20
	v_fma_f32 v20, v16, v20, v16
	v_mul_f32_e32 v20, 0x3f4c422a, v20
	v_cmp_nlt_f32_e64 s[12:13], |v20|, s29
	s_and_saveexec_b64 s[42:43], s[12:13]
	s_xor_b64 s[12:13], exec, s[42:43]
	s_cbranch_execz .LBB0_1507
	v_add_f32_e64 v24, |v20|, |v20|
	v_mul_f32_e32 v25, 0x3fb8aa3b, v24
	v_rndne_f32_e32 v26, v25
	v_sub_f32_e32 v27, v25, v26
	v_fma_f32 v25, v24, s33, -v25
	v_fmac_f32_e32 v25, 0x32a5705f, v24
	v_add_f32_e32 v25, v27, v25
	v_cvt_i32_f32_e32 v26, v26
	v_exp_f32_e32 v25, v25
	v_cmp_ngt_f32_e32 vcc, s36, v24
	v_ldexp_f32 v25, v25, v26
	s_nop 0
	v_cndmask_b32_e32 v25, 0, v25, vcc
	v_cmp_nlt_f32_e32 vcc, s37, v24
	s_nop 1
	v_cndmask_b32_e32 v24, v77, v25, vcc
	v_add_f32_e32 v24, 1.0, v24
	v_rcp_f32_e32 v24, v24
	s_nop 0
	v_fma_f32 v24, v24, -2.0, 1.0

.LBB0_1519:
	s_andn2_saveexec_b64 s[12:13], s[12:13]
	v_mul_f32_e32 v27, v23, v23
	v_fmamk_f32 v28, v27, 0xbbbac73d, v75
	v_fmaak_f32 v28, v27, v28, 0xbd5c1c4e
	v_fmaak_f32 v28, v27, v28, 0x3e088382
	v_fmaak_f32 v28, v27, v28, 0xbeaaaa99
	v_mul_f32_e64 v28, |v23|, v28
	v_fma_f32 v27, v27, v28, |v23|
	s_or_b64 exec, exec, s[12:13]
	v_bfi_b32 v20, s38, v24, v20
	v_mul_f32_e32 v16, 0.5, v16
	v_add_f32_e32 v20, 1.0, v20
	v_bfi_b32 v22, s38, v26, v22
	v_bfi_b32 v21, s38, v25, v21
	v_mul_f32_e32 v16, v16, v20
	v_bfi_b32 v20, s38, v27, v23
	v_mul_f32_e32 v18, 0.5, v18
	v_add_f32_e32 v22, 1.0, v22
	v_mul_f32_e32 v17, 0.5, v17
	v_add_f32_e32 v21, 1.0, v21
	v_mul_f32_e32 v19, 0.5, v19
	v_add_f32_e32 v20, 1.0, v20
	v_mul_f32_e32 v18, v18, v22
	v_mul_f32_e32 v17, v17, v21
	v_mul_f32_e32 v19, v19, v20
	v_cvt_pk_bf16_f32 v16, v16, v17
	v_cvt_pk_bf16_f32 v17, v18, v19
	global_store_dwordx2 v[34:35], v[16:17], off offset:96
	v_mov_b32_e32 v16, v160
	v_mov_b32_e32 v17, v161
	v_mov_b32_e32 v18, v162
	v_mov_b32_e32 v19, v163
	v_add_f32_e32 v12, v12, v16
	v_mul_f32_e32 v16, 0x3d372713, v12
	v_mul_f32_e32 v16, v12, v16
	v_fma_f32 v16, v12, v16, v12
	v_mul_f32_e32 v16, 0x3f4c422a, v16
	v_cmp_nlt_f32_e64 s[12:13], |v16|, s29
	s_and_saveexec_b64 s[42:43], s[12:13]
	s_xor_b64 s[12:13], exec, s[42:43]
	s_cbranch_execz .LBB0_1523
	v_add_f32_e64 v20, |v16|, |v16|
	v_mul_f32_e32 v21, 0x3fb8aa3b, v20
	v_rndne_f32_e32 v22, v21
	v_sub_f32_e32 v23, v21, v22
	v_fma_f32 v21, v20, s33, -v21
	v_fmac_f32_e32 v21, 0x32a5705f, v20
	v_add_f32_e32 v21, v23, v21
	v_cvt_i32_f32_e32 v22, v22
	v_exp_f32_e32 v21, v21
	v_cmp_ngt_f32_e32 vcc, s36, v20
	v_ldexp_f32 v21, v21, v22
	s_nop 0
	v_cndmask_b32_e32 v21, 0, v21, vcc
	v_cmp_nlt_f32_e32 vcc, s37, v20
	s_nop 1
	v_cndmask_b32_e32 v20, v77, v21, vcc
	v_add_f32_e32 v20, 1.0, v20
	v_rcp_f32_e32 v20, v20
	s_nop 0
	v_fma_f32 v20, v20, -2.0, 1.0

.LBB0_1535:
	s_andn2_saveexec_b64 s[12:13], s[12:13]
	v_mul_f32_e32 v23, v19, v19
	v_fmamk_f32 v24, v23, 0xbbbac73d, v75
	v_fmaak_f32 v24, v23, v24, 0xbd5c1c4e
	v_fmaak_f32 v24, v23, v24, 0x3e088382
	v_fmaak_f32 v24, v23, v24, 0xbeaaaa99
	v_mul_f32_e64 v24, |v19|, v24
	v_fma_f32 v23, v23, v24, |v19|
	s_or_b64 exec, exec, s[12:13]
	v_bfi_b32 v18, s38, v22, v18
	v_bfi_b32 v17, s38, v21, v17
	v_mul_f32_e32 v14, 0.5, v14
	v_add_f32_e32 v18, 1.0, v18
	v_mul_f32_e32 v13, 0.5, v13
	v_add_f32_e32 v17, 1.0, v17
	v_mul_f32_e32 v14, v14, v18
	v_mul_f32_e32 v18, v13, v17
	v_bfi_b32 v13, s38, v20, v16
	v_mul_f32_e32 v12, 0.5, v12
	v_add_f32_e32 v13, 1.0, v13
	v_mul_f32_e32 v20, v12, v13
	v_or_b32_e32 v12, s40, v36
	v_add3_u32 v12, v37, v12, 16
	v_ashrrev_i32_e32 v13, 31, v12
	v_lshlrev_b64 v[12:13], 8, v[12:13]
	v_lshl_add_u64 v[12:13], s[10:11], 0, v[12:13]
	v_lshl_add_u64 v[16:17], v[12:13], 0, v[64:65]
	v_bfi_b32 v13, s38, v23, v19
	v_mul_f32_e32 v12, 0.5, v15
	v_add_f32_e32 v13, 1.0, v13
	v_mul_f32_e32 v13, v12, v13
	v_cvt_pk_bf16_f32 v12, v20, v18
	v_cvt_pk_bf16_f32 v13, v14, v13
	global_store_dwordx2 v[16:17], v[12:13], off
	v_mov_b32_e32 v12, v164
	v_mov_b32_e32 v13, v165
	v_mov_b32_e32 v14, v166
	v_mov_b32_e32 v15, v167
	v_add_f32_e32 v8, v8, v12
	v_mul_f32_e32 v12, 0x3d372713, v8
	v_mul_f32_e32 v12, v8, v12
	v_fma_f32 v12, v8, v12, v8
	v_mul_f32_e32 v12, 0x3f4c422a, v12
	v_cmp_nlt_f32_e64 s[10:11], |v12|, s29
	s_and_saveexec_b64 s[12:13], s[10:11]
	s_xor_b64 s[10:11], exec, s[12:13]
	s_cbranch_execz .LBB0_1539
	v_add_f32_e64 v18, |v12|, |v12|
	v_mul_f32_e32 v19, 0x3fb8aa3b, v18
	v_rndne_f32_e32 v20, v19
	v_sub_f32_e32 v21, v19, v20
	v_fma_f32 v19, v18, s33, -v19
	v_fmac_f32_e32 v19, 0x32a5705f, v18
	v_add_f32_e32 v19, v21, v19
	v_cvt_i32_f32_e32 v20, v20
	v_exp_f32_e32 v19, v19
	v_cmp_ngt_f32_e32 vcc, s36, v18
	v_ldexp_f32 v19, v19, v20
	s_nop 0
	v_cndmask_b32_e32 v19, 0, v19, vcc
	v_cmp_nlt_f32_e32 vcc, s37, v18
	s_nop 1
	v_cndmask_b32_e32 v18, v77, v19, vcc
	v_add_f32_e32 v18, 1.0, v18
	v_rcp_f32_e32 v18, v18
	s_nop 0
	v_fma_f32 v18, v18, -2.0, 1.0

.LBB0_1551:
	s_andn2_saveexec_b64 s[10:11], s[10:11]
	v_mul_f32_e32 v21, v15, v15
	v_fmamk_f32 v22, v21, 0xbbbac73d, v75
	v_fmaak_f32 v22, v21, v22, 0xbd5c1c4e
	v_fmaak_f32 v22, v21, v22, 0x3e088382
	v_fmaak_f32 v22, v21, v22, 0xbeaaaa99
	v_mul_f32_e64 v22, |v15|, v22
	v_fma_f32 v21, v21, v22, |v15|
	s_or_b64 exec, exec, s[10:11]
	v_bfi_b32 v12, s38, v18, v12
	v_mul_f32_e32 v8, 0.5, v8
	v_add_f32_e32 v12, 1.0, v12
	v_bfi_b32 v14, s38, v20, v14
	v_bfi_b32 v13, s38, v19, v13
	v_mul_f32_e32 v8, v8, v12
	v_bfi_b32 v12, s38, v21, v15
	v_mul_f32_e32 v10, 0.5, v10
	v_add_f32_e32 v14, 1.0, v14
	v_mul_f32_e32 v9, 0.5, v9
	v_add_f32_e32 v13, 1.0, v13
	v_mul_f32_e32 v11, 0.5, v11
	v_add_f32_e32 v12, 1.0, v12
	v_mul_f32_e32 v10, v10, v14
	v_mul_f32_e32 v9, v9, v13
	v_mul_f32_e32 v11, v11, v12
	v_cvt_pk_bf16_f32 v8, v8, v9
	v_cvt_pk_bf16_f32 v9, v10, v11
	global_store_dwordx2 v[16:17], v[8:9], off offset:32
	v_mov_b32_e32 v8, v168
	v_mov_b32_e32 v9, v169
	v_mov_b32_e32 v10, v170
	v_mov_b32_e32 v11, v171
	v_add_f32_e32 v4, v4, v8
	v_mul_f32_e32 v8, 0x3d372713, v4
	v_mul_f32_e32 v8, v4, v8
	v_fma_f32 v8, v4, v8, v4
	v_mul_f32_e32 v8, 0x3f4c422a, v8
	v_cmp_nlt_f32_e64 s[10:11], |v8|, s29
	s_and_saveexec_b64 s[12:13], s[10:11]
	s_xor_b64 s[10:11], exec, s[12:13]
	s_cbranch_execz .LBB0_1555
	v_add_f32_e64 v12, |v8|, |v8|
	v_mul_f32_e32 v13, 0x3fb8aa3b, v12
	v_rndne_f32_e32 v14, v13
	v_sub_f32_e32 v15, v13, v14
	v_fma_f32 v13, v12, s33, -v13
	v_fmac_f32_e32 v13, 0x32a5705f, v12
	v_add_f32_e32 v13, v15, v13
	v_cvt_i32_f32_e32 v14, v14
	v_exp_f32_e32 v13, v13
	v_cmp_ngt_f32_e32 vcc, s36, v12
	v_ldexp_f32 v13, v13, v14
	s_nop 0
	v_cndmask_b32_e32 v13, 0, v13, vcc
	v_cmp_nlt_f32_e32 vcc, s37, v12
	s_nop 1
	v_cndmask_b32_e32 v12, v77, v13, vcc
	v_add_f32_e32 v12, 1.0, v12
	v_rcp_f32_e32 v12, v12
	s_nop 0
	v_fma_f32 v12, v12, -2.0, 1.0

.LBB0_1567:
	s_andn2_saveexec_b64 s[10:11], s[10:11]
	v_mul_f32_e32 v15, v11, v11
	v_fmamk_f32 v18, v15, 0xbbbac73d, v75
	v_fmaak_f32 v18, v15, v18, 0xbd5c1c4e
	v_fmaak_f32 v18, v15, v18, 0x3e088382
	v_fmaak_f32 v18, v15, v18, 0xbeaaaa99
	v_mul_f32_e64 v18, |v11|, v18
	v_fma_f32 v15, v15, v18, |v11|
	s_or_b64 exec, exec, s[10:11]
	v_bfi_b32 v8, s38, v12, v8
	v_mul_f32_e32 v4, 0.5, v4
	v_add_f32_e32 v8, 1.0, v8
	v_bfi_b32 v10, s38, v14, v10
	v_bfi_b32 v9, s38, v13, v9
	v_mul_f32_e32 v4, v4, v8
	v_bfi_b32 v8, s38, v15, v11
	v_mul_f32_e32 v6, 0.5, v6
	v_add_f32_e32 v10, 1.0, v10
	v_mul_f32_e32 v5, 0.5, v5
	v_add_f32_e32 v9, 1.0, v9
	v_mul_f32_e32 v7, 0.5, v7
	v_add_f32_e32 v8, 1.0, v8
	v_mul_f32_e32 v6, v6, v10
	v_mul_f32_e32 v5, v5, v9
	v_mul_f32_e32 v7, v7, v8
	v_cvt_pk_bf16_f32 v4, v4, v5
	v_cvt_pk_bf16_f32 v5, v6, v7
	global_store_dwordx2 v[16:17], v[4:5], off offset:64
	v_mov_b32_e32 v4, v172
	v_mov_b32_e32 v5, v173
	v_mov_b32_e32 v6, v174
	v_mov_b32_e32 v7, v175
	v_add_f32_e32 v0, v0, v4
	v_mul_f32_e32 v4, 0x3d372713, v0
	v_mul_f32_e32 v4, v0, v4
	v_fma_f32 v4, v0, v4, v0
	v_mul_f32_e32 v4, 0x3f4c422a, v4
	v_cmp_nlt_f32_e64 s[10:11], |v4|, s29
	s_and_saveexec_b64 s[12:13], s[10:11]
	s_xor_b64 s[10:11], exec, s[12:13]
	s_cbranch_execz .LBB0_1571
	v_add_f32_e64 v8, |v4|, |v4|
	v_mul_f32_e32 v9, 0x3fb8aa3b, v8
	v_rndne_f32_e32 v10, v9
	v_sub_f32_e32 v11, v9, v10
	v_fma_f32 v9, v8, s33, -v9
	v_fmac_f32_e32 v9, 0x32a5705f, v8
	v_add_f32_e32 v9, v11, v9
	v_cvt_i32_f32_e32 v10, v10
	v_exp_f32_e32 v9, v9
	v_cmp_ngt_f32_e32 vcc, s36, v8
	v_ldexp_f32 v9, v9, v10
	s_nop 0
	v_cndmask_b32_e32 v9, 0, v9, vcc
	v_cmp_nlt_f32_e32 vcc, s37, v8
	s_nop 1
	v_cndmask_b32_e32 v8, v77, v9, vcc
	v_add_f32_e32 v8, 1.0, v8
	v_rcp_f32_e32 v8, v8
	s_nop 0
	v_fma_f32 v8, v8, -2.0, 1.0
